# speedup vs baseline: 1.0747x; 1.0085x over previous
.LBB5_7:
	s_load_dwordx2 s[2:3], s[0:1], 0x38
	v_lshrrev_b32_e32 v1, 1, v0
	v_bfe_u32 v138, v0, 5, 1
	v_and_b32_e32 v142, 0xc0, v1
	v_lshlrev_b32_e32 v1, 7, v139
	v_and_b32_e32 v140, 31, v0
	v_and_b32_e32 v141, 0x80, v1
	v_or_b32_e32 v1, 2, v138
	s_and_b64 vcc, exec, s[14:15]
	s_cbranch_vccz .LBB5_20
	v_or_b32_e32 v2, v142, v140
	v_bitop3_b32 v4, v1, v11, 3 bitop3:0x78
	v_lshlrev_b32_e32 v144, 6, v2
	v_lshlrev_b32_e32 v146, 4, v4
	v_or_b32_e32 v2, v141, v140
	v_add_u32_e32 v4, s16, v11
	v_lshlrev_b32_e32 v147, 6, v2
	v_min_i32_e32 v2, s24, v4
	v_mul_lo_u32 v2, s6, v2
	v_bitop3_b32 v3, v138, v11, 3 bitop3:0x78
	v_add3_u32 v2, v2, s9, v10
	v_lshlrev_b32_e32 v145, 4, v3
	v_ashrrev_i32_e32 v3, 31, v2
	v_lshl_add_u64 v[2:3], v[2:3], 1, s[4:5]
	s_mov_b64 s[26:27], 0xc0
	v_lshl_add_u64 v[130:131], v[2:3], 0, s[26:27]
	v_add_u32_e32 v2, 0x80, v4
	v_min_i32_e32 v2, s24, v2
	v_mul_lo_u32 v2, s6, v2
	v_add3_u32 v2, v2, s9, v10
	v_ashrrev_i32_e32 v3, 31, v2
	s_mul_i32 s19, s19, s21
	v_lshl_add_u64 v[2:3], v[2:3], 1, s[4:5]
	s_sub_i32 s4, s22, s19
	s_sub_i32 s4, s4, s23
	s_mul_i32 s4, s10, s4
	s_lshl_b32 s4, s4, 8
	s_lshl_b32 s5, s20, 8
	s_add_i32 s5, s5, s4
	v_or_b32_e32 v4, s5, v11
	v_lshl_add_u64 v[132:133], v[2:3], 0, s[26:27]
	v_mul_lo_u32 v2, s8, v4
	v_add3_u32 v2, v2, s9, v10
	v_ashrrev_i32_e32 v3, 31, v2
	v_lshl_add_u64 v[2:3], v[2:3], 1, s[12:13]
	v_lshl_add_u64 v[134:135], v[2:3], 0, s[26:27]
	v_or_b32_e32 v2, 0x80, v4
	v_mul_lo_u32 v2, s8, v2
	v_add3_u32 v2, v2, s9, v10
	v_ashrrev_i32_e32 v3, 31, v2
	v_lshl_add_u64 v[2:3], v[2:3], 1, s[12:13]
	v_lshl_add_u64 v[136:137], v[2:3], 0, s[26:27]
	v_mov_b32_e32 v2, 0
	s_mov_b32 s14, 3
	s_add_i32 s15, s18, -1
	s_mov_b32 s6, 0
	s_mov_b64 s[4:5], 0
	s_mov_b32 s10, 3
	v_mov_b32_e32 v3, v2
	v_mov_b32_e32 v4, v2
	v_mov_b32_e32 v5, v2
	v_mov_b32_e32 v6, v2
	v_mov_b32_e32 v7, v2
	v_mov_b32_e32 v8, v2
	v_mov_b32_e32 v9, v2
	v_mov_b32_e32 v10, v2
	v_mov_b32_e32 v11, v2
	v_mov_b32_e32 v12, v2
	v_mov_b32_e32 v13, v2
	v_mov_b32_e32 v14, v2
	v_mov_b32_e32 v15, v2
	v_mov_b32_e32 v16, v2
	v_mov_b32_e32 v17, v2
	v_mov_b32_e32 v18, v2
	v_mov_b32_e32 v19, v2
	v_mov_b32_e32 v20, v2
	v_mov_b32_e32 v21, v2
	v_mov_b32_e32 v22, v2
	v_mov_b32_e32 v23, v2
	v_mov_b32_e32 v24, v2
	v_mov_b32_e32 v25, v2
	v_mov_b32_e32 v26, v2
	v_mov_b32_e32 v27, v2
	v_mov_b32_e32 v28, v2
	v_mov_b32_e32 v29, v2
	v_mov_b32_e32 v30, v2
	v_mov_b32_e32 v31, v2
	v_mov_b32_e32 v32, v2
	v_mov_b32_e32 v33, v2
	v_mov_b32_e32 v34, v2
	v_mov_b32_e32 v35, v2
	v_mov_b32_e32 v36, v2
	v_mov_b32_e32 v37, v2
	v_mov_b32_e32 v38, v2
	v_mov_b32_e32 v39, v2
	v_mov_b32_e32 v40, v2
	v_mov_b32_e32 v41, v2
	v_mov_b32_e32 v42, v2
	v_mov_b32_e32 v43, v2
	v_mov_b32_e32 v44, v2
	v_mov_b32_e32 v45, v2
	v_mov_b32_e32 v46, v2
	v_mov_b32_e32 v47, v2
	v_mov_b32_e32 v48, v2
	v_mov_b32_e32 v49, v2
	v_mov_b32_e32 v50, v2
	v_mov_b32_e32 v51, v2
	v_mov_b32_e32 v52, v2
	v_mov_b32_e32 v53, v2
	v_mov_b32_e32 v54, v2
	v_mov_b32_e32 v55, v2
	v_mov_b32_e32 v56, v2
	v_mov_b32_e32 v57, v2
	v_mov_b32_e32 v58, v2
	v_mov_b32_e32 v59, v2
	v_mov_b32_e32 v60, v2
	v_mov_b32_e32 v61, v2
	v_mov_b32_e32 v62, v2
	v_mov_b32_e32 v63, v2
	v_mov_b32_e32 v64, v2
	v_mov_b32_e32 v65, v2
	v_mov_b32_e32 v66, v2
	v_mov_b32_e32 v67, v2
	v_mov_b32_e32 v68, v2
	v_mov_b32_e32 v69, v2
	v_mov_b32_e32 v70, v2
	v_mov_b32_e32 v71, v2
	v_mov_b32_e32 v72, v2
	v_mov_b32_e32 v73, v2
	v_mov_b32_e32 v74, v2
	v_mov_b32_e32 v75, v2
	v_mov_b32_e32 v76, v2
	v_mov_b32_e32 v77, v2
	v_mov_b32_e32 v78, v2
	v_mov_b32_e32 v79, v2
	v_mov_b32_e32 v80, v2
	v_mov_b32_e32 v81, v2
	v_mov_b32_e32 v82, v2
	v_mov_b32_e32 v83, v2
	v_mov_b32_e32 v84, v2
	v_mov_b32_e32 v85, v2
	v_mov_b32_e32 v86, v2
	v_mov_b32_e32 v87, v2
	v_mov_b32_e32 v88, v2
	v_mov_b32_e32 v89, v2
	v_mov_b32_e32 v90, v2
	v_mov_b32_e32 v91, v2
	v_mov_b32_e32 v92, v2
	v_mov_b32_e32 v93, v2
	v_mov_b32_e32 v94, v2
	v_mov_b32_e32 v95, v2
	v_mov_b32_e32 v96, v2
	v_mov_b32_e32 v97, v2
	v_mov_b32_e32 v98, v2
	v_mov_b32_e32 v99, v2
	v_mov_b32_e32 v100, v2
	v_mov_b32_e32 v101, v2
	v_mov_b32_e32 v102, v2
	v_mov_b32_e32 v103, v2
	v_mov_b32_e32 v104, v2
	v_mov_b32_e32 v105, v2
	v_mov_b32_e32 v106, v2
	v_mov_b32_e32 v107, v2
	v_mov_b32_e32 v108, v2
	v_mov_b32_e32 v109, v2
	v_mov_b32_e32 v110, v2
	v_mov_b32_e32 v111, v2
	v_mov_b32_e32 v112, v2
	v_mov_b32_e32 v113, v2
	v_mov_b32_e32 v114, v2
	v_mov_b32_e32 v115, v2
	v_mov_b32_e32 v116, v2
	v_mov_b32_e32 v117, v2
	v_mov_b32_e32 v118, v2
	v_mov_b32_e32 v119, v2
	v_mov_b32_e32 v120, v2
	v_mov_b32_e32 v121, v2
	v_mov_b32_e32 v122, v2
	v_mov_b32_e32 v123, v2
	v_mov_b32_e32 v124, v2
	v_mov_b32_e32 v125, v2
	v_mov_b32_e32 v126, v2
	v_mov_b32_e32 v127, v2
	v_mov_b32_e32 v128, v2
	v_mov_b32_e32 v129, v2
	v_readfirstlane_b32 s28, v143
	v_add_u32_e32 v172, v144, v145
	v_add_u32_e32 v173, v144, v146
	v_add_u32_e32 v144, v147, v145
	v_add_u32_e32 v147, v147, v146
	v_mov_b32_e32 v145, v172
	v_mov_b32_e32 v146, v173
	s_mov_b32 s9, 0x18000
	s_or_b32 m0, s9, s28
	s_nop 0
	global_load_lds_dwordx4 v[130:131], off
	v_lshl_add_u64 v[130:131], v[130:131], 0, 64
	s_add_u32 m0, m0, 0x2000
	global_load_lds_dwordx4 v[132:133], off
	v_lshl_add_u64 v[132:133], v[132:133], 0, 64
	s_add_u32 m0, m0, 0x2000
	global_load_lds_dwordx4 v[134:135], off
	v_lshl_add_u64 v[134:135], v[134:135], 0, 64
	s_add_u32 m0, m0, 0x2000
	global_load_lds_dwordx4 v[136:137], off
	v_lshl_add_u64 v[136:137], v[136:137], 0, 64
	s_mov_b32 s10, 4
	s_waitcnt vmcnt(12)
	s_barrier
	s_cmp_ge_u32 s28, 0x1000
	s_cbranch_scc1 .Lk5_hi
	ds_read_b128 v[148:151], v145
	ds_read_b128 v[152:155], v144 offset:16384
	ds_read_b128 v[160:163], v144 offset:18432
	ds_read_b128 v[156:159], v145 offset:2048
	ds_read_b128 v[164:167], v144 offset:20480
	ds_read_b128 v[168:171], v144 offset:22528

.Lk5_hi:
	s_waitcnt vmcnt(8)
	s_waitcnt lgkmcnt(0)
	s_barrier
	s_lshl_b32 s8, s6, 15
	v_add_u32_e32 v174, s8, v145
	v_add_u32_e32 v175, s8, v144
	ds_read_b128 v[148:151], v174
	ds_read_b128 v[152:155], v175 offset:16384
	ds_read_b128 v[160:163], v175 offset:18432
	ds_read_b128 v[156:159], v174 offset:2048
	ds_read_b128 v[164:167], v175 offset:20480
	ds_read_b128 v[168:171], v175 offset:22528
	v_add_u32_e32 v172, s8, v146
	v_add_u32_e32 v173, s8, v147
	s_waitcnt lgkmcnt(0)
	ds_read_b128 v[176:179], v172
	ds_read_b128 v[184:187], v173 offset:16384
	ds_read_b128 v[188:191], v173 offset:18432
	ds_read_b128 v[180:183], v172 offset:2048
	ds_read_b128 v[192:195], v173 offset:20480
	ds_read_b128 v[196:199], v173 offset:22528
	s_lshl_b32 s9, s10, 15
	s_or_b32 m0, s9, s28
	v_mfma_f32_32x32x16_f16 v[114:129], v[148:151], v[152:155], v[114:129]
	global_load_lds_dwordx4 v[130:131], off
	v_lshl_add_u64 v[130:131], v[130:131], 0, 64
	s_add_u32 m0, m0, 0x2000
	v_mfma_f32_32x32x16_f16 v[98:113], v[148:151], v[160:163], v[98:113]
	global_load_lds_dwordx4 v[132:133], off
	v_lshl_add_u64 v[132:133], v[132:133], 0, 64
	s_add_u32 m0, m0, 0x2000
	v_mfma_f32_32x32x16_f16 v[82:97], v[148:151], v[164:167], v[82:97]
	global_load_lds_dwordx4 v[134:135], off
	v_lshl_add_u64 v[134:135], v[134:135], 0, 64
	s_add_u32 m0, m0, 0x2000
	v_mfma_f32_32x32x16_f16 v[66:81], v[148:151], v[168:171], v[66:81]
	global_load_lds_dwordx4 v[136:137], off
	v_lshl_add_u64 v[136:137], v[136:137], 0, 64
	v_mfma_f32_32x32x16_f16 v[50:65], v[156:159], v[152:155], v[50:65]
	v_mfma_f32_32x32x16_f16 v[34:49], v[156:159], v[160:163], v[34:49]
	v_mfma_f32_32x32x16_f16 v[18:33], v[156:159], v[164:167], v[18:33]
	v_mfma_f32_32x32x16_f16 v[2:17], v[156:159], v[168:171], v[2:17]
	s_add_i32 s6, s6, 1
	s_cmp_eq_u32 s6, 5
	s_cselect_b32 s6, 0, s6
	s_add_i32 s10, s10, 1
	s_cmp_eq_u32 s10, 5
	s_cselect_b32 s10, 0, s10
.Lk5_hloop:
	s_waitcnt vmcnt(8)
	s_waitcnt lgkmcnt(0)
	s_barrier
	s_lshl_b32 s8, s6, 15
	v_add_u32_e32 v174, s8, v145
	v_add_u32_e32 v175, s8, v144
	ds_read_b128 v[148:151], v174
	ds_read_b128 v[152:155], v175 offset:16384
	ds_read_b128 v[160:163], v175 offset:18432
	ds_read_b128 v[156:159], v174 offset:2048
	ds_read_b128 v[164:167], v175 offset:20480
	ds_read_b128 v[168:171], v175 offset:22528
	v_add_u32_e32 v172, s8, v146
	v_add_u32_e32 v173, s8, v147
	v_mfma_f32_32x32x16_f16 v[114:129], v[176:179], v[184:187], v[114:129]
	v_mfma_f32_32x32x16_f16 v[98:113], v[176:179], v[188:191], v[98:113]
	v_mfma_f32_32x32x16_f16 v[82:97], v[176:179], v[192:195], v[82:97]
	v_mfma_f32_32x32x16_f16 v[66:81], v[176:179], v[196:199], v[66:81]
	v_mfma_f32_32x32x16_f16 v[50:65], v[180:183], v[184:187], v[50:65]
	v_mfma_f32_32x32x16_f16 v[34:49], v[180:183], v[188:191], v[34:49]
	v_mfma_f32_32x32x16_f16 v[18:33], v[180:183], v[192:195], v[18:33]
	v_mfma_f32_32x32x16_f16 v[2:17], v[180:183], v[196:199], v[2:17]
	s_waitcnt lgkmcnt(0)
	ds_read_b128 v[176:179], v172
	ds_read_b128 v[184:187], v173 offset:16384
	ds_read_b128 v[188:191], v173 offset:18432
	ds_read_b128 v[180:183], v172 offset:2048
	ds_read_b128 v[192:195], v173 offset:20480
	ds_read_b128 v[196:199], v173 offset:22528
	s_lshl_b32 s9, s10, 15
	s_or_b32 m0, s9, s28
	v_mfma_f32_32x32x16_f16 v[114:129], v[148:151], v[152:155], v[114:129]
	global_load_lds_dwordx4 v[130:131], off
	v_lshl_add_u64 v[130:131], v[130:131], 0, 64
	s_add_u32 m0, m0, 0x2000
	v_mfma_f32_32x32x16_f16 v[98:113], v[148:151], v[160:163], v[98:113]
	global_load_lds_dwordx4 v[132:133], off
	v_lshl_add_u64 v[132:133], v[132:133], 0, 64
	s_add_u32 m0, m0, 0x2000
	v_mfma_f32_32x32x16_f16 v[82:97], v[148:151], v[164:167], v[82:97]
	global_load_lds_dwordx4 v[134:135], off
	v_lshl_add_u64 v[134:135], v[134:135], 0, 64
	s_add_u32 m0, m0, 0x2000
	v_mfma_f32_32x32x16_f16 v[66:81], v[148:151], v[168:171], v[66:81]
	global_load_lds_dwordx4 v[136:137], off
	v_lshl_add_u64 v[136:137], v[136:137], 0, 64
	v_mfma_f32_32x32x16_f16 v[50:65], v[156:159], v[152:155], v[50:65]
	v_mfma_f32_32x32x16_f16 v[34:49], v[156:159], v[160:163], v[34:49]
	v_mfma_f32_32x32x16_f16 v[18:33], v[156:159], v[164:167], v[18:33]
	v_mfma_f32_32x32x16_f16 v[2:17], v[156:159], v[168:171], v[2:17]
	s_add_i32 s6, s6, 1
	s_cmp_eq_u32 s6, 5
	s_cselect_b32 s6, 0, s6
	s_add_i32 s10, s10, 1
	s_cmp_eq_u32 s10, 5
	s_cselect_b32 s10, 0, s10
	s_add_i32 s15, s15, -1
	s_cmp_lg_u32 s15, 0
	s_cbranch_scc1 .Lk5_hloop
	s_waitcnt lgkmcnt(0)
	v_mfma_f32_32x32x16_f16 v[114:129], v[176:179], v[184:187], v[114:129]
	v_mfma_f32_32x32x16_f16 v[98:113], v[176:179], v[188:191], v[98:113]
	v_mfma_f32_32x32x16_f16 v[82:97], v[176:179], v[192:195], v[82:97]
	v_mfma_f32_32x32x16_f16 v[66:81], v[176:179], v[196:199], v[66:81]
	v_mfma_f32_32x32x16_f16 v[50:65], v[180:183], v[184:187], v[50:65]
	v_mfma_f32_32x32x16_f16 v[34:49], v[180:183], v[188:191], v[34:49]
	v_mfma_f32_32x32x16_f16 v[18:33], v[180:183], v[192:195], v[18:33]
	v_mfma_f32_32x32x16_f16 v[2:17], v[180:183], v[196:199], v[2:17]
	s_branch .LBB5_21
